# baseline (speedup 1.0000x reference)
.LBB0_35:
	s_or_b64 exec, exec, s[0:1]
	s_sleep 16
	s_waitcnt vmcnt(14)
	v_mul_u32_u24_e32 v105, 0x880, v227
	s_waitcnt vmcnt(11)
	v_cvt_pk_f16_f32 v3, v150, v151
	v_cvt_pk_f16_f32 v2, v148, v149
	v_lshl_add_u32 v4, v1, 1, v105
	s_waitcnt vmcnt(10)
	v_cvt_pk_f16_f32 v1, v154, v155
	s_waitcnt lgkmcnt(0)
	v_cvt_pk_f16_f32 v0, v152, v153
	s_barrier
	v_lshl_or_b32 v233, v225, 6, v220
	v_mul_u32_u24_e32 v233, 0x110, v233
	v_add_u32_e32 v233, v233, v223
	v_add_u32_e32 v233, 0x10000, v233
	ds_read_b128 v[180:183], v233
	ds_read_b128 v[184:187], v233 offset:32
	ds_read_b128 v[188:191], v233 offset:64
	ds_read_b128 v[192:195], v233 offset:96
	ds_read_b128 v[196:199], v233 offset:128
	ds_read_b128 v[200:203], v233 offset:160
	ds_read_b128 v[204:207], v233 offset:192
	ds_read_b128 v[208:211], v233 offset:224
	ds_write2_b64 v4, v[2:3], v[0:1] offset1:34
	s_waitcnt vmcnt(9)
	v_cvt_pk_f16_f32 v1, v166, v167
	v_cvt_pk_f16_f32 v0, v164, v165
	s_waitcnt vmcnt(8)
	v_cvt_pk_f16_f32 v3, v158, v159
	v_cvt_pk_f16_f32 v2, v156, v157
	ds_write2_b64 v4, v[0:1], v[2:3] offset0:68 offset1:102
	s_waitcnt vmcnt(7)
	v_cvt_pk_f16_f32 v1, v162, v163
	v_cvt_pk_f16_f32 v0, v160, v161
	s_waitcnt vmcnt(6)
	v_cvt_pk_f16_f32 v3, v170, v171
	v_cvt_pk_f16_f32 v2, v168, v169
	ds_write2_b64 v4, v[0:1], v[2:3] offset0:136 offset1:170
	s_waitcnt vmcnt(5)
	v_cvt_pk_f16_f32 v1, v174, v175
	v_cvt_pk_f16_f32 v0, v172, v173
	s_waitcnt vmcnt(4)
	v_cvt_pk_f16_f32 v3, v178, v179
	v_cvt_pk_f16_f32 v2, v176, v177
	ds_write2_b64 v4, v[0:1], v[2:3] offset0:204 offset1:238
	ds_read_b128 v[148:151], v233 offset:8704
	ds_read_b128 v[152:155], v233 offset:8736
	ds_read_b128 v[156:159], v233 offset:8768
	ds_read_b128 v[160:163], v233 offset:8800
	ds_read_b128 v[164:167], v233 offset:8832
	ds_read_b128 v[168:171], v233 offset:8864
	ds_read_b128 v[172:175], v233 offset:8896
	ds_read_b128 v[176:179], v233 offset:8928
	v_lshlrev_b32_e32 v2, 1, v228
	s_waitcnt vmcnt(1)
	v_cvt_pk_f16_f32 v1, v40, v41
	v_cvt_pk_f16_f32 v0, v38, v39
	v_mad_u32_u24 v3, v227, s6, v2
	ds_write_b64 v3, v[0:1] offset:34816
	s_waitcnt vmcnt(0)
	v_cvt_pk_f16_f32 v1, v36, v37
	v_cvt_pk_f16_f32 v0, v34, v35
	v_mad_u32_u24 v2, v229, s6, v2
	ds_write_b64 v2, v[0:1] offset:34816
	v_mov_b32_e32 v97, 0
	v_mov_b32_e32 v0, 0
	v_mov_b32_e32 v4, 0
	v_mov_b32_e32 v96, 0
	s_and_saveexec_b64 s[0:1], vcc
	s_cbranch_execz .LBB0_37
	v_lshl_add_u32 v1, v220, 1, v230
	v_or_b32_e32 v2, 0x21000, v1
	v_add_u32_e32 v1, 0x21040, v1
	ds_read_u16 v1, v1
	ds_read_u16 v2, v2
	v_cvt_f16_f32_e32 v0, v104
	s_waitcnt lgkmcnt(1)
	v_and_b32_e32 v4, 0xffff, v1
	v_pack_b32_f16 v0, v0, 0
	s_waitcnt lgkmcnt(0)
	v_and_b32_e32 v96, 0xffff, v2
